# expert weight conversion of layers 1-3 moved out of the prologue: early workgroups convert during barrier waits after ragged phases, the rest one item per wave at the other barriers
# speedup vs baseline: 1.0143x; 1.0143x over previous
.Lcvt_site_0:
	s_mov_b32 s31, 0
	s_branch .Lcvt_post
.Lcvt_site_1:
	s_mov_b32 s31, 1
	s_branch .Lcvt_post
.Lcvt_site_2:
	s_mov_b32 s31, 2
	s_branch .Lcvt_post

.Lcvt_site_4:
	s_mov_b32 s31, 4
	s_branch .Lcvt_post

.Lcvt_site_6:
	s_mov_b32 s31, 6
	s_branch .Lcvt_post
.Lcvt_site_7:
	s_mov_b32 s31, 7
	s_branch .Lcvt_post
.Lcvt_site_8:
	s_mov_b32 s31, 8
	s_branch .Lcvt_post

.Lcvt_post:
	s_mov_b64 exec, -1
	v_lshrrev_b32_e32 v2, 6, v0
	v_and_b32_e32 v3, 63, v0
	s_nop 0
	v_readfirstlane_b32 s25, v2
	s_nop 3
	s_cmp_eq_u32 s31, 5
	s_cbranch_scc0 .Lcvt_s10
	s_cmp_ge_u32 s62, 3
	s_cbranch_scc1 .Lcvt_ret
	s_sub_i32 s27, s80, 16
	s_cmp_lt_i32 s27, 0
	s_cbranch_scc1 .Lcvt_ret
	s_mov_b32 s26, 3
	s_movk_i32 s30, 0
	s_branch .Lcvt_go
.Lcvt_s10:
	s_cmp_eq_u32 s31, 10
	s_cbranch_scc0 .Lcvt_s9
	s_cmp_ge_u32 s62, 3
	s_cbranch_scc1 .Lcvt_ret
	s_sub_i32 s27, s63, 112
	s_cmp_lt_i32 s27, 0
	s_cbranch_scc1 .Lcvt_ret
	s_mov_b32 s26, 4
	s_movk_i32 s30, 5040
	s_branch .Lcvt_go
.Lcvt_s9:
	s_cmp_eq_u32 s31, 9
	s_cbranch_scc0 .Lcvt_s3
	s_cmp_ge_u32 s62, 3
	s_cbranch_scc1 .Lcvt_ret
	s_sub_i32 s27, s63, 208
	s_cmp_lt_i32 s27, 0
	s_cbranch_scc1 .Lcvt_ret
	s_mov_b32 s26, 3
	s_movk_i32 s30, 9072
	s_branch .Lcvt_go
.Lcvt_s3:
	s_cmp_eq_u32 s31, 3
	s_cbranch_scc0 .Lcvt_lock
	s_cmp_ge_u32 s62, 3
	s_cbranch_scc1 .Lcvt_ret
	s_sub_i32 s27, s63, 208
	s_cmp_lt_i32 s27, 0
	s_cbranch_scc1 .Lcvt_ret
	s_mov_b32 s26, 1
	s_movk_i32 s30, 10080
	s_branch .Lcvt_go
.Lcvt_lock:
	s_mov_b32 s27, s31
	s_cmp_ge_u32 s31, 4
	s_cselect_b32 s26, 1, 0
	s_sub_i32 s27, s27, s26
	s_cmp_ge_u32 s31, 6
	s_cselect_b32 s26, 1, 0
	s_sub_i32 s27, s27, s26
	s_mul_i32 s26, s62, 7
	s_add_i32 s27, s27, s26
	s_mul_i32 s27, s27, 0x700
	s_mul_i32 s26, s80, 7
	s_add_i32 s27, s27, s26
	s_add_i32 s27, s27, s25
	s_add_i32 s27, s27, -1
	s_cmp_ge_u32 s27, 0xa800
	s_cbranch_scc1 .Lcvt_ret
	s_mov_b32 s26, 1
	s_cmpk_ge_u32 s27, 0x3800
	s_cbranch_scc0 .Lcvt_lk
	s_add_i32 s27, s27, 0xffffc800
	s_mov_b32 s26, 2
	s_cmpk_ge_u32 s27, 0x3800
	s_cbranch_scc0 .Lcvt_lk
	s_add_i32 s27, s27, 0xffffc800
	s_mov_b32 s26, 3
.Lcvt_lk:
	s_add_i32 s30, s27, 10240
	s_mov_b32 s27, s26
	s_mov_b32 s26, 1
	s_movk_i32 s4, 0x6000
	s_branch .Lcvt_lanes
.Lcvt_go:
	s_mul_i32 s27, s27, 7
	s_add_i32 s27, s27, s25
	s_add_i32 s27, s27, -1
	s_mul_i32 s27, s27, s26
	s_add_i32 s30, s30, s27
	s_add_i32 s27, s62, 1
	s_movk_i32 s4, 10240
.Lcvt_lanes:
	v_lshrrev_b32_e32 v4, 3, v3
	v_and_b32_e32 v5, 7, v3
	v_mul_u32_u24_e32 v7, 17, v4
	v_and_b32_e32 v8, 3, v3
	v_lshl_add_u32 v7, v8, 2, v7
	v_lshlrev_b32_e32 v7, 2, v7
	v_mul_u32_u24_e32 v8, 0x110, v5
	v_add_lshl_u32 v8, v8, v4, 2
	s_mul_i32 s17, s25, 0x2200
	v_add_u32_e32 v7, s17, v7
	v_add_u32_e32 v8, s17, v8
	v_lshlrev_b32_e32 v9, 10, v4
	v_lshl_add_u32 v9, v5, 4, v9
	v_add_u32_e32 v10, 0x2000, v9
.Lcvt_item:
	s_cmp_ge_u32 s30, s4
	s_cbranch_scc1 .Lcvt_ret
	s_mov_b32 s6, s27
	s_mov_b32 s5, s30
	s_lshr_b32 s7, s5, 8
	s_mul_i32 s7, s7, 0xaaab
	s_lshr_b32 s7, s7, 17
	s_mul_i32 s8, s7, 0x300
	s_sub_i32 s8, s5, s8
	s_lshl_b32 s9, s6, 5
	s_add_i32 s9, s9, s7
	s_load_dwordx2 s[2:3], s[0:1], 0x100
	s_mov_b32 s18, s9
	s_mov_b32 s19, 0
	s_cmp_lt_u32 s8, 0x200
	s_cbranch_scc0 .Lcvt_dn
	s_load_dwordx2 s[10:11], s[0:1], 0xd8
	s_lshr_b32 s12, s8, 6
	s_and_b32 s13, s8, 63
	s_lshr_b32 s14, s13, 2
	s_and_b32 s14, s14, 7
	s_lshl_b32 s14, s14, 3
	s_and_b32 s15, s13, 3
	s_add_i32 s14, s14, s15
	s_lshr_b32 s15, s13, 5
	s_lshl_b32 s15, s15, 2
	s_add_i32 s14, s14, s15
	s_mov_b32 s16, 13
	s_lshl_b64 s[20:21], s[18:19], 23
	s_lshl_b64 s[22:23], s[18:19], 21
	s_mov_b32 s24, 0x6000000
	s_branch .Lcvt_common
